# hybrid K1: each wave streams 15 private contiguous 16KiB chunks (baseline-like mapping), then pulls the remaining 1/6 of the matrix from 16 atomic chunk queues; 8KiB load bursts
# speedup vs baseline: 1.0304x; 1.0304x over previous
.Lk1_scan:
	s_load_dwordx2 s[4:5], s[0:1], 0x0
	s_load_dwordx4 s[8:11], s[0:1], 0x20
	s_load_dwordx2 s[12:13], s[0:1], 0x30
	v_and_b32_e32 v6, 63, v0
	v_readfirstlane_b32 s3, v0
	v_lshlrev_b32_e32 v1, 4, v6
	v_lshlrev_b32_e32 v2, 2, v6
	v_or_b32_e32 v3, 1, v2
	v_or_b32_e32 v4, 2, v2
	v_or_b32_e32 v5, 3, v2
	s_lshr_b32 s3, s3, 6
	s_sub_u32 s16, s2, 0x60
	s_lshl_b32 s16, s16, 2
	s_add_u32 s16, s16, s3
	s_mul_i32 s17, s16, 0x48000
	s_lshr_b32 s18, s17, 2
	s_lshl_b32 s24, s3, 13
	s_mov_b32 s25, s24
	s_mov_b32 s28, s24
	s_mov_b32 s36, 0
	v_mov_b32_e32 v21, 1
	s_mov_b32 s27, 0
	s_mov_b32 s29, 0x55555556
	s_mov_b32 s31, 0xc0000
	s_waitcnt lgkmcnt(0)
	s_and_b32 s50, s16, 15
	s_mul_i32 s52, s50, 384
	s_add_u32 s52, s52, 30720
	s_lshl_b32 s53, s50, 6
	s_add_u32 s53, s53, 0xe000
	s_add_u32 s54, s10, s53
	s_addc_u32 s55, s11, 0
	s_mul_i32 s59, s16, 15
	s_mul_i32 s57, s59, 0x4000
	s_lshr_b32 s18, s57, 2
	s_add_u32 s6, s4, s57
	s_addc_u32 s7, s5, 0
	v_mov_b32_e32 v27, 0
	global_load_dwordx4 v[28:31], v1, s[6:7] nt
	s_add_u32 s6, s6, 0x400
	s_addc_u32 s7, s7, 0
	global_load_dwordx4 v[32:35], v1, s[6:7] nt
	s_add_u32 s6, s6, 0x400
	s_addc_u32 s7, s7, 0
	global_load_dwordx4 v[36:39], v1, s[6:7] nt
	s_add_u32 s6, s6, 0x400
	s_addc_u32 s7, s7, 0
	global_load_dwordx4 v[40:43], v1, s[6:7] nt
	s_add_u32 s6, s6, 0x400
	s_addc_u32 s7, s7, 0
	global_load_dwordx4 v[44:47], v1, s[6:7] nt
	s_add_u32 s6, s6, 0x400
	s_addc_u32 s7, s7, 0
	global_load_dwordx4 v[48:51], v1, s[6:7] nt
	s_add_u32 s6, s6, 0x400
	s_addc_u32 s7, s7, 0
	global_load_dwordx4 v[52:55], v1, s[6:7] nt
	s_add_u32 s6, s6, 0x400
	s_addc_u32 s7, s7, 0
	global_load_dwordx4 v[56:59], v1, s[6:7] nt
	s_add_u32 s6, s6, 0x400
	s_addc_u32 s7, s7, 0
	global_load_dwordx4 v[60:63], v1, s[6:7] nt
	s_add_u32 s6, s6, 0x400
	s_addc_u32 s7, s7, 0
	global_load_dwordx4 v[64:67], v1, s[6:7] nt
	s_add_u32 s6, s6, 0x400
	s_addc_u32 s7, s7, 0
	global_load_dwordx4 v[68:71], v1, s[6:7] nt
	s_add_u32 s6, s6, 0x400
	s_addc_u32 s7, s7, 0
	global_load_dwordx4 v[72:75], v1, s[6:7] nt
	s_add_u32 s6, s6, 0x400
	s_addc_u32 s7, s7, 0
	global_load_dwordx4 v[76:79], v1, s[6:7] nt
	s_add_u32 s6, s6, 0x400
	s_addc_u32 s7, s7, 0
	global_load_dwordx4 v[80:83], v1, s[6:7] nt
	s_add_u32 s6, s6, 0x400
	s_addc_u32 s7, s7, 0
	global_load_dwordx4 v[84:87], v1, s[6:7] nt
	s_add_u32 s6, s6, 0x400
	s_addc_u32 s7, s7, 0
	global_load_dwordx4 v[88:91], v1, s[6:7] nt
	s_add_u32 s6, s6, 0x400
	s_addc_u32 s7, s7, 0
	s_mov_b32 s26, 18
	s_add_u32 s57, s59, 1
	s_mul_i32 s57, s57, 0x4000
	s_lshr_b32 s58, s57, 2
	s_add_u32 s6, s4, s57
	s_addc_u32 s7, s5, 0
	s_mov_b32 s26, 0

.Lk1_contm_15:
	global_load_dwordx4 v[60:63], v1, s[6:7] nt
	s_add_u32 s6, s6, 0x400
	s_addc_u32 s7, s7, 0
	global_load_dwordx4 v[64:67], v1, s[6:7] nt
	s_add_u32 s6, s6, 0x400
	s_addc_u32 s7, s7, 0
	global_load_dwordx4 v[68:71], v1, s[6:7] nt
	s_add_u32 s6, s6, 0x400
	s_addc_u32 s7, s7, 0
	global_load_dwordx4 v[72:75], v1, s[6:7] nt
	s_add_u32 s6, s6, 0x400
	s_addc_u32 s7, s7, 0
	global_load_dwordx4 v[76:79], v1, s[6:7] nt
	s_add_u32 s6, s6, 0x400
	s_addc_u32 s7, s7, 0
	global_load_dwordx4 v[80:83], v1, s[6:7] nt
	s_add_u32 s6, s6, 0x400
	s_addc_u32 s7, s7, 0
	global_load_dwordx4 v[84:87], v1, s[6:7] nt
	s_add_u32 s6, s6, 0x400
	s_addc_u32 s7, s7, 0
	global_load_dwordx4 v[88:91], v1, s[6:7] nt
	s_add_u32 s6, s6, 0x400
	s_addc_u32 s7, s7, 0
	s_mov_b32 s18, s58
	s_add_u32 s60, s26, 2
	s_cmp_lt_u32 s60, 15
	s_cbranch_scc0 .Lk1_dynid
	s_add_u32 s57, s59, s60
	s_branch .Lk1_haveid
.Lk1_dynid:
	v_readfirstlane_b32 s56, v26
	s_nop 0
	s_cmp_lt_u32 s56, 384
	s_cbranch_scc0 .Lk1_lastchunk
	s_add_u32 s57, s52, s56
.Lk1_haveid:
	s_mul_i32 s57, s57, 0x4000
	s_lshr_b32 s58, s57, 2
	s_add_u32 s6, s4, s57
	s_addc_u32 s7, s5, 0
	s_add_u32 s60, s26, 3
	s_cmp_lt_u32 s60, 15
	s_cbranch_scc1 .Lk1_noreq
	s_mov_b64 exec, 1
	global_atomic_add v26, v27, v21, s[54:55] sc0
	s_mov_b64 exec, -1
.Lk1_noreq:
	s_add_u32 s26, s26, 1
	s_branch .Lk1_main
